# stack27 = stack23 + router-logit loops: exact counted waits on the back edge (no wait for the previous step's H2 stores), one full wait in the first step
# speedup vs baseline: 1.0090x; 1.0039x over previous
; DEVINL unsigned pk2(float lo, float hi) { const f32x2 v = {lo, hi}; return __builtin_bit_cast(unsigned, __builtin_convertvector(v, bf16v2)); }
; DEVINL float bflo(unsigned u) { return __uint_as_float(u << 16); }
; DEVINL void phase4(const Params& P, unsigned char* smem) {
;     ...
;             for (int p = 0; p < 4; ++p) {
;                 union { bf16x8 v; unsigned u[4]; } hh[2], hl[2];
;                 unsigned h8[2][2];
; #pragma unroll
;                 for (int q = 0; q < 2; ++q) {
;                     const int nt = 2 * p + q, col = 128 * wv + 16 * nt + 4 * g;
;                     const f32x4 mul = *(const f32x4*)(s_t2 + col), sh = *(const f32x4*)(s_t3 + col);
; #pragma unroll
;                     for (int mi2 = 0; mi2 < 2; ++mi2) {
;                         const f32x4 h = xl[(nt * 2 + mi2) * 512] * rt2[mi2] * mul + sh;
;                         const unsigned u01 = pk2(h.x, h.y), u23 = pk2(h.z, h.w);
;                         hh[mi2].u[2 * q] = u01; hh[mi2].u[2 * q + 1] = u23;
;                         hl[mi2].u[2 * q] = pk2(h.x - bflo(u01), h.y - bfhi(u01));
;                         hl[mi2].u[2 * q + 1] = pk2(h.z - bflo(u23), h.w - bfhi(u23));
;                         h8[q][mi2] = pk4_fp8(h.x, h.y, h.z, h.w);
;                     }
;                 }
;                 __builtin_amdgcn_sched_barrier(0);
; #pragma unroll
;                 for (int ot = 0; ot < 3; ++ot) {
;                     const bf16x8 whi = rwh[ot], wlo = rwl[ot];
; #pragma unroll
;                     for (int mi2 = 0; mi2 < 2; ++mi2) {
;                         f32x4 a = lg[ot][2 * hf + mi2];
;                         a = __builtin_amdgcn_mfma_f32_16x16x32_bf16(whi, hh[mi2].v, a, 0, 0, 0);
;                         a = __builtin_amdgcn_mfma_f32_16x16x32_bf16(whi, hl[mi2].v, a, 0, 0, 0);
;                         a = __builtin_amdgcn_mfma_f32_16x16x32_bf16(wlo, hh[mi2].v, a, 0, 0, 0);
;                         lg[ot][2 * hf + mi2] = a;
;                     }
;                 }
;                 __builtin_amdgcn_sched_barrier(0);
;                 { const int pn = p < 3 ? p + 1 : 3;
; #pragma unroll
;                   for (int ot = 0; ot < 3; ++ot) { rwh[ot] = *(const bf16x8*)(wr + (size_t)(pn * 3 + ot) * 512); rwl[ot] = *(const bf16x8*)(wr + (size_t)(4 * 8 * 3 * 64) * 8 + (size_t)(pn * 3 + ot) * 512); } }
.LBB0_596:
	v_add_u32_e32 v215, s0, v135
	v_add_u32_e32 v114, 0x22000, v215
	ds_read_b128 v[120:123], v114
	v_add_u32_e32 v114, 0x23000, v215
	ds_read_b128 v[124:127], v114
	ds_read_b128 v[114:117], v245
	ds_read_b128 v[226:229], v245 offset:8192
	v_mov_b32_e32 v214, 0
	s_waitcnt lgkmcnt(1)
	v_pk_mul_f32 v[116:117], v[204:205], v[116:117]
	v_pk_mul_f32 v[114:115], v[190:191], v[114:115]
	v_pk_fma_f32 v[116:117], v[122:123], v[116:117], v[126:127]
	v_pk_fma_f32 v[128:129], v[120:121], v[114:115], v[124:125]
	v_cvt_pk_bf16_f32 v115, v116, v117
	v_cvt_pk_bf16_f32 v114, v128, v129
	v_lshlrev_b32_e32 v118, 16, v114
	v_and_b32_e32 v119, 0xffff0000, v114
	v_lshlrev_b32_e32 v212, 16, v115
	v_and_b32_e32 v213, 0xffff0000, v115
	v_pk_add_f32 v[118:119], v[128:129], v[118:119] neg_lo:[0,1] neg_hi:[0,1]
	v_pk_add_f32 v[212:213], v[116:117], v[212:213] neg_lo:[0,1] neg_hi:[0,1]
	v_cvt_pk_bf16_f32 v118, v118, v119
	v_cvt_pk_bf16_f32 v119, v212, v213
	v_mov_b32_e32 v212, 0
	v_cvt_pk_fp8_f32 v212, v128, v129
	s_waitcnt lgkmcnt(0)
	v_pk_mul_f32 v[128:129], v[202:203], v[226:227]
	v_mov_b32_e32 v213, 0
	v_pk_fma_f32 v[120:121], v[120:121], v[128:129], v[124:125]
	v_cvt_pk_fp8_f32 v212, v116, v117 op_sel:[0,0,1]
	v_pk_mul_f32 v[116:117], v[206:207], v[228:229]
	v_cvt_pk_fp8_f32 v214, v120, v121
	v_pk_fma_f32 v[116:117], v[122:123], v[116:117], v[126:127]
	v_cvt_pk_bf16_f32 v122, v120, v121
	v_lshlrev_b32_e32 v124, 16, v122
	v_and_b32_e32 v125, 0xffff0000, v122
	v_cvt_pk_bf16_f32 v123, v116, v117
	v_pk_add_f32 v[124:125], v[120:121], v[124:125] neg_lo:[0,1] neg_hi:[0,1]
	v_cvt_pk_fp8_f32 v214, v116, v117 op_sel:[0,0,1]
	v_cvt_pk_bf16_f32 v126, v124, v125
	v_lshlrev_b32_e32 v124, 16, v123
	v_and_b32_e32 v125, 0xffff0000, v123
	v_pk_add_f32 v[124:125], v[116:117], v[124:125] neg_lo:[0,1] neg_hi:[0,1]
	v_add_u32_e32 v116, 0x22040, v215
	ds_read_b128 v[226:229], v116
	v_add_u32_e32 v116, 0x23040, v215
	ds_read_b128 v[230:233], v116
	ds_read_b128 v[234:237], v245 offset:16384
	v_cvt_pk_bf16_f32 v127, v124, v125
	v_mov_b32_e32 v215, 0
	s_waitcnt lgkmcnt(0)
	v_pk_mul_f32 v[116:117], v[204:205], v[236:237]
	v_pk_mul_f32 v[120:121], v[190:191], v[234:235]
	v_pk_fma_f32 v[124:125], v[228:229], v[116:117], v[232:233]
	v_pk_fma_f32 v[128:129], v[226:227], v[120:121], v[230:231]
	v_cvt_pk_bf16_f32 v117, v124, v125
	v_cvt_pk_bf16_f32 v116, v128, v129
	v_lshlrev_b32_e32 v120, 16, v116
	v_and_b32_e32 v121, 0xffff0000, v116
	v_lshlrev_b32_e32 v234, 16, v117
	v_and_b32_e32 v235, 0xffff0000, v117
	v_pk_add_f32 v[120:121], v[128:129], v[120:121] neg_lo:[0,1] neg_hi:[0,1]
	v_pk_add_f32 v[234:235], v[124:125], v[234:235] neg_lo:[0,1] neg_hi:[0,1]
	v_cvt_pk_bf16_f32 v120, v120, v121
	v_cvt_pk_bf16_f32 v121, v234, v235
	ds_read_b128 v[234:237], v245 offset:24576
	v_cvt_pk_fp8_f32 v213, v128, v129
	s_waitcnt lgkmcnt(0)
	v_pk_mul_f32 v[128:129], v[202:203], v[234:235]
	v_cvt_pk_fp8_f32 v213, v124, v125 op_sel:[0,0,1]
	v_pk_mul_f32 v[124:125], v[206:207], v[236:237]
	v_pk_fma_f32 v[226:227], v[226:227], v[128:129], v[230:231]
	v_pk_fma_f32 v[228:229], v[228:229], v[124:125], v[232:233]
	v_cvt_pk_fp8_f32 v215, v226, v227
	v_cvt_pk_bf16_f32 v124, v226, v227
	v_cvt_pk_bf16_f32 v125, v228, v229
	v_lshlrev_b32_e32 v128, 16, v124
	v_and_b32_e32 v129, 0xffff0000, v124
	v_lshlrev_b32_e32 v230, 16, v125
	v_and_b32_e32 v231, 0xffff0000, v125
	v_pk_add_f32 v[128:129], v[226:227], v[128:129] neg_lo:[0,1] neg_hi:[0,1]
	v_pk_add_f32 v[230:231], v[228:229], v[230:231] neg_lo:[0,1] neg_hi:[0,1]
	v_cvt_pk_bf16_f32 v128, v128, v129
	v_cvt_pk_bf16_f32 v129, v230, v231
	v_cvt_pk_fp8_f32 v215, v228, v229 op_sel:[0,0,1]
	s_cmp_lg_u32 s0, 0
	s_cbranch_scc1 .Lrt_steady0
	s_waitcnt vmcnt(0)
.Lrt_steady0:
	s_waitcnt vmcnt(7)
	v_mfma_f32_16x16x32_bf16 v[82:85], v[94:97], v[114:117], v[82:85]
	v_mfma_f32_16x16x32_bf16 v[86:89], v[94:97], v[122:125], v[86:89]
	s_waitcnt vmcnt(6)
	v_mfma_f32_16x16x32_bf16 v[78:81], v[90:93], v[114:117], v[78:81]
	v_mfma_f32_16x16x32_bf16 v[74:77], v[90:93], v[122:125], v[74:77]
	s_waitcnt vmcnt(4)
	v_mfma_f32_16x16x32_bf16 v[70:73], v[98:101], v[114:117], v[70:73]
	v_mfma_f32_16x16x32_bf16 v[66:69], v[98:101], v[122:125], v[66:69]
	v_mfma_f32_16x16x32_bf16 v[82:85], v[94:97], v[118:121], v[82:85]
	v_mfma_f32_16x16x32_bf16 v[86:89], v[94:97], v[126:129], v[86:89]
	v_mfma_f32_16x16x32_bf16 v[78:81], v[90:93], v[118:121], v[78:81]
	v_mfma_f32_16x16x32_bf16 v[74:77], v[90:93], v[126:129], v[74:77]
	v_mfma_f32_16x16x32_bf16 v[70:73], v[98:101], v[118:121], v[70:73]
	v_mfma_f32_16x16x32_bf16 v[66:69], v[98:101], v[126:129], v[66:69]
	v_mfma_f32_16x16x32_bf16 v[82:85], v[106:109], v[114:117], v[82:85]
	v_mfma_f32_16x16x32_bf16 v[86:89], v[106:109], v[122:125], v[86:89]
	s_waitcnt vmcnt(3)
	v_mfma_f32_16x16x32_bf16 v[78:81], v[110:113], v[114:117], v[78:81]
	v_mfma_f32_16x16x32_bf16 v[74:77], v[110:113], v[122:125], v[74:77]
	s_waitcnt vmcnt(2)
	v_mfma_f32_16x16x32_bf16 v[70:73], v[102:105], v[114:117], v[70:73]
	v_mfma_f32_16x16x32_bf16 v[66:69], v[102:105], v[122:125], v[66:69]
	s_cmpk_eq_i32 s0, 0x180
	s_cbranch_scc1 .Lrt_skip0
	s_cmpk_lg_i32 s0, 0x180
	s_cselect_b32 s24, s1, 0x1200
	s_lshl_b64 s[14:15], s[24:25], 1
	v_lshl_add_u64 v[98:99], v[130:131], 0, s[14:15]
	v_lshl_add_u64 v[100:101], v[132:133], 0, s[14:15]
	s_add_i32 s14, s24, 0x200
	s_mov_b32 s15, s25
	s_addk_i32 s24, 0x400
	v_lshl_add_u64 v[102:103], s[14:15], 1, v[132:133]
	v_lshl_add_u64 v[104:105], s[24:25], 1, v[132:133]
	global_load_dwordx4 v[94:97], v[98:99], off
	global_load_dwordx4 v[90:93], v[98:99], off offset:1024
	global_load_dwordx4 v[106:109], v[100:101], off
	s_nop 0
	global_load_dwordx4 v[98:101], v[98:99], off offset:2048
	s_nop 0
	global_load_dwordx4 v[110:113], v[102:103], off
	s_nop 0
	global_load_dwordx4 v[102:105], v[104:105], off

; DEVINL unsigned pk2(float lo, float hi) { const f32x2 v = {lo, hi}; return __builtin_bit_cast(unsigned, __builtin_convertvector(v, bf16v2)); }
; DEVINL float bflo(unsigned u) { return __uint_as_float(u << 16); }
; DEVINL void phase4(const Params& P, unsigned char* smem) {
;     ...
;             for (int p = 0; p < 4; ++p) {
;                 union { bf16x8 v; unsigned u[4]; } hh[2], hl[2];
;                 unsigned h8[2][2];
; #pragma unroll
;                 for (int q = 0; q < 2; ++q) {
;                     const int nt = 2 * p + q, col = 128 * wv + 16 * nt + 4 * g;
;                     const f32x4 mul = *(const f32x4*)(s_t2 + col), sh = *(const f32x4*)(s_t3 + col);
; #pragma unroll
;                     for (int mi2 = 0; mi2 < 2; ++mi2) {
;                         const f32x4 h = xl[(nt * 2 + mi2) * 512] * rt2[mi2] * mul + sh;
;                         const unsigned u01 = pk2(h.x, h.y), u23 = pk2(h.z, h.w);
;                         hh[mi2].u[2 * q] = u01; hh[mi2].u[2 * q + 1] = u23;
;                         hl[mi2].u[2 * q] = pk2(h.x - bflo(u01), h.y - bfhi(u01));
;                         hl[mi2].u[2 * q + 1] = pk2(h.z - bflo(u23), h.w - bfhi(u23));
;                         h8[q][mi2] = pk4_fp8(h.x, h.y, h.z, h.w);
;                     }
;                 }
;                 __builtin_amdgcn_sched_barrier(0);
; #pragma unroll
;                 for (int ot = 0; ot < 3; ++ot) {
;                     const bf16x8 whi = rwh[ot], wlo = rwl[ot];
; #pragma unroll
;                     for (int mi2 = 0; mi2 < 2; ++mi2) {
;                         f32x4 a = lg[ot][2 * hf + mi2];
;                         a = __builtin_amdgcn_mfma_f32_16x16x32_bf16(whi, hh[mi2].v, a, 0, 0, 0);
;                         a = __builtin_amdgcn_mfma_f32_16x16x32_bf16(whi, hl[mi2].v, a, 0, 0, 0);
;                         a = __builtin_amdgcn_mfma_f32_16x16x32_bf16(wlo, hh[mi2].v, a, 0, 0, 0);
;                         lg[ot][2 * hf + mi2] = a;
;                     }
;                 }
;                 __builtin_amdgcn_sched_barrier(0);
;                 { const int pn = p < 3 ? p + 1 : 3;
; #pragma unroll
;                   for (int ot = 0; ot < 3; ++ot) { rwh[ot] = *(const bf16x8*)(wr + (size_t)(pn * 3 + ot) * 512); rwl[ot] = *(const bf16x8*)(wr + (size_t)(4 * 8 * 3 * 64) * 8 + (size_t)(pn * 3 + ot) * 512); } }
.LBB0_603:
	v_add_u32_e32 v63, s0, v135
	v_add_u32_e32 v64, 0x22000, v63
	v_add_u32_e32 v65, 0x23000, v63
	ds_read_b128 v[90:93], v62
	ds_read_b128 v[94:97], v64
	s_waitcnt vmcnt(10)
	ds_read_b128 v[98:101], v65
	s_waitcnt vmcnt(8)
	ds_read_b128 v[102:105], v62 offset:8192
	v_mov_b32_e32 v122, 0
	s_waitcnt lgkmcnt(3)
	v_pk_mul_f32 v[64:65], v[54:55], v[92:93]
	v_pk_mul_f32 v[90:91], v[50:51], v[90:91]
	s_waitcnt lgkmcnt(1)
	v_pk_fma_f32 v[64:65], v[96:97], v[64:65], v[100:101]
	v_pk_fma_f32 v[92:93], v[94:95], v[90:91], v[98:99]
	v_cvt_pk_bf16_f32 v91, v64, v65
	v_cvt_pk_bf16_f32 v90, v92, v93
	v_lshlrev_b32_e32 v106, 16, v90
	v_and_b32_e32 v107, 0xffff0000, v90
	v_lshlrev_b32_e32 v108, 16, v91
	v_cvt_pk_fp8_f32 v122, v92, v93
	v_and_b32_e32 v109, 0xffff0000, v91
	v_pk_add_f32 v[106:107], v[92:93], v[106:107] neg_lo:[0,1] neg_hi:[0,1]
	v_pk_add_f32 v[92:93], v[64:65], v[108:109] neg_lo:[0,1] neg_hi:[0,1]
	v_cvt_pk_bf16_f32 v106, v106, v107
	v_cvt_pk_bf16_f32 v107, v92, v93
	s_waitcnt lgkmcnt(0)
	v_pk_mul_f32 v[92:93], v[52:53], v[102:103]
	v_cvt_pk_fp8_f32 v122, v64, v65 op_sel:[0,0,1]
	v_pk_fma_f32 v[92:93], v[94:95], v[92:93], v[98:99]
	v_pk_mul_f32 v[64:65], v[56:57], v[104:105]
	v_cvt_pk_bf16_f32 v94, v92, v93
	v_pk_fma_f32 v[64:65], v[96:97], v[64:65], v[100:101]
	v_lshlrev_b32_e32 v96, 16, v94
	v_and_b32_e32 v97, 0xffff0000, v94
	v_mov_b32_e32 v104, 0
	v_pk_add_f32 v[96:97], v[92:93], v[96:97] neg_lo:[0,1] neg_hi:[0,1]
	v_cvt_pk_fp8_f32 v104, v92, v93
	v_add_u32_e32 v92, 0x22040, v63
	v_add_u32_e32 v63, 0x23040, v63
	ds_read_b128 v[100:103], v62 offset:16384
	ds_read_b128 v[110:113], v92
	ds_read_b128 v[114:117], v63
	v_cvt_pk_bf16_f32 v95, v64, v65
	v_cvt_pk_bf16_f32 v98, v96, v97
	v_lshlrev_b32_e32 v96, 16, v95
	v_and_b32_e32 v97, 0xffff0000, v95
	v_pk_add_f32 v[96:97], v[64:65], v[96:97] neg_lo:[0,1] neg_hi:[0,1]
	s_waitcnt lgkmcnt(2)
	v_pk_mul_f32 v[92:93], v[50:51], v[100:101]
	v_cvt_pk_bf16_f32 v99, v96, v97
	s_waitcnt lgkmcnt(0)
	v_pk_fma_f32 v[96:97], v[110:111], v[92:93], v[114:115]
	v_cvt_pk_fp8_f32 v104, v64, v65 op_sel:[0,0,1]
	ds_read_b128 v[118:121], v62 offset:24576
	v_pk_mul_f32 v[64:65], v[54:55], v[102:103]
	v_cvt_pk_bf16_f32 v92, v96, v97
	v_pk_fma_f32 v[64:65], v[112:113], v[64:65], v[116:117]
	v_lshlrev_b32_e32 v100, 16, v92
	v_and_b32_e32 v101, 0xffff0000, v92
	v_cvt_pk_bf16_f32 v93, v64, v65
	v_pk_add_f32 v[100:101], v[96:97], v[100:101] neg_lo:[0,1] neg_hi:[0,1]
	v_mov_b32_e32 v123, 0
	v_cvt_pk_bf16_f32 v108, v100, v101
	v_lshlrev_b32_e32 v100, 16, v93
	v_cvt_pk_fp8_f32 v123, v96, v97
	v_and_b32_e32 v101, 0xffff0000, v93
	v_pk_add_f32 v[96:97], v[64:65], v[100:101] neg_lo:[0,1] neg_hi:[0,1]
	v_mov_b32_e32 v105, 0
	v_cvt_pk_bf16_f32 v109, v96, v97
	s_waitcnt lgkmcnt(0)
	v_pk_mul_f32 v[96:97], v[52:53], v[118:119]
	v_cvt_pk_fp8_f32 v123, v64, v65 op_sel:[0,0,1]
	v_pk_fma_f32 v[100:101], v[110:111], v[96:97], v[114:115]
	v_pk_mul_f32 v[64:65], v[56:57], v[120:121]
	v_cvt_pk_fp8_f32 v105, v100, v101
	v_pk_fma_f32 v[64:65], v[112:113], v[64:65], v[116:117]
	v_cvt_pk_bf16_f32 v96, v100, v101
	v_cvt_pk_bf16_f32 v97, v64, v65
	v_lshlrev_b32_e32 v102, 16, v96
	v_and_b32_e32 v103, 0xffff0000, v96
	v_pk_add_f32 v[100:101], v[100:101], v[102:103] neg_lo:[0,1] neg_hi:[0,1]
	v_lshlrev_b32_e32 v102, 16, v97
	v_and_b32_e32 v103, 0xffff0000, v97
	v_cvt_pk_fp8_f32 v105, v64, v65 op_sel:[0,0,1]
	v_pk_add_f32 v[64:65], v[64:65], v[102:103] neg_lo:[0,1] neg_hi:[0,1]
	v_cvt_pk_bf16_f32 v100, v100, v101
	v_cvt_pk_bf16_f32 v101, v64, v65
	s_cmp_lg_u32 s0, 0
	s_cbranch_scc1 .Lrt_steady1
	s_waitcnt vmcnt(0)
.Lrt_steady1:
	s_waitcnt vmcnt(7)
	v_mfma_f32_16x16x32_bf16 v[18:21], v[30:33], v[90:93], v[18:21]
	v_mfma_f32_16x16x32_bf16 v[22:25], v[30:33], v[94:97], v[22:25]
	s_waitcnt vmcnt(6)
	v_mfma_f32_16x16x32_bf16 v[14:17], v[26:29], v[90:93], v[14:17]
	v_mfma_f32_16x16x32_bf16 v[10:13], v[26:29], v[94:97], v[10:13]
	s_waitcnt vmcnt(4)
	v_mfma_f32_16x16x32_bf16 v[6:9], v[34:37], v[90:93], v[6:9]
	v_mfma_f32_16x16x32_bf16 v[2:5], v[34:37], v[94:97], v[2:5]
	v_mfma_f32_16x16x32_bf16 v[18:21], v[30:33], v[106:109], v[18:21]
	v_mfma_f32_16x16x32_bf16 v[22:25], v[30:33], v[98:101], v[22:25]
	v_mfma_f32_16x16x32_bf16 v[14:17], v[26:29], v[106:109], v[14:17]
	v_mfma_f32_16x16x32_bf16 v[10:13], v[26:29], v[98:101], v[10:13]
	v_mfma_f32_16x16x32_bf16 v[6:9], v[34:37], v[106:109], v[6:9]
	v_mfma_f32_16x16x32_bf16 v[2:5], v[34:37], v[98:101], v[2:5]
	v_mfma_f32_16x16x32_bf16 v[18:21], v[42:45], v[90:93], v[18:21]
	v_mfma_f32_16x16x32_bf16 v[22:25], v[42:45], v[94:97], v[22:25]
	s_waitcnt vmcnt(3)
	v_mfma_f32_16x16x32_bf16 v[14:17], v[46:49], v[90:93], v[14:17]
	v_mfma_f32_16x16x32_bf16 v[10:13], v[46:49], v[94:97], v[10:13]
	s_waitcnt vmcnt(2)
	v_mfma_f32_16x16x32_bf16 v[6:9], v[38:41], v[90:93], v[6:9]
	v_mfma_f32_16x16x32_bf16 v[2:5], v[38:41], v[94:97], v[2:5]
	s_cmpk_eq_i32 s0, 0x180
	s_cbranch_scc1 .Lrt_skip1
	s_cmpk_lg_i32 s0, 0x180
	s_cselect_b32 s24, s1, 0x1200
	s_lshl_b64 s[8:9], s[24:25], 1
	v_lshl_add_u64 v[34:35], v[130:131], 0, s[8:9]
	v_lshl_add_u64 v[36:37], v[132:133], 0, s[8:9]
	s_add_i32 s8, s24, 0x200
	s_mov_b32 s9, s25
	s_addk_i32 s24, 0x400
	v_lshl_add_u64 v[38:39], s[8:9], 1, v[132:133]
	v_lshl_add_u64 v[40:41], s[24:25], 1, v[132:133]
	global_load_dwordx4 v[30:33], v[34:35], off
	global_load_dwordx4 v[26:29], v[34:35], off offset:1024
	global_load_dwordx4 v[42:45], v[36:37], off
	s_nop 0
	global_load_dwordx4 v[34:37], v[34:35], off offset:2048
	s_nop 0
	global_load_dwordx4 v[46:49], v[38:39], off
	s_nop 0
	global_load_dwordx4 v[38:41], v[40:41], off
